# streaming tile loads use sc0 sc1 nt cache policy instead of nt
# speedup vs baseline: 1.0111x; 1.0111x over previous
_Z10k_attn_epiILi2EEvPKfS1_PKiPKDF16_S5_PfS1_S1_S5_S1_S1_S1_S1_S1_S6_:
	s_load_dwordx8 s[12:19], s[0:1], 0x0
	s_load_dwordx2 s[4:5], s[0:1], 0x20
	s_load_dwordx4 s[20:23], s[0:1], 0x30
	v_and_b32_e32 v196, 63, v0
	v_cmp_gt_u32_e64 s[6:7], 32, v196
	s_waitcnt lgkmcnt(0)
	v_mov_b32_e32 v1, s15
	v_mov_b32_e32 v2, s13
	v_lshrrev_b32_e32 v197, 6, v0
	s_lshl_b32 s31, s2, 3
	v_cndmask_b32_e64 v103, v1, v2, s[6:7]
	v_mov_b32_e32 v1, s14
	v_mov_b32_e32 v2, s12
	v_or_b32_e32 v104, s31, v197
	v_cndmask_b32_e64 v102, v1, v2, s[6:7]
	s_mov_b32 s8, 0x19000
	v_lshlrev_b32_e32 v1, 4, v0
	v_mad_i64_i32 v[2:3], s[2:3], v104, s8, v[102:103]
	v_and_b32_e32 v108, 0x1f0, v1
	v_mov_b32_e32 v109, 0
	v_lshl_add_u64 v[14:15], v[2:3], 0, v[108:109]
	v_mov_b32_e32 v2, s23
	v_mov_b32_e32 v3, s21
	v_ashrrev_i32_e32 v105, 31, v104
	v_cndmask_b32_e64 v3, v2, v3, s[6:7]
	v_mov_b32_e32 v2, s22
	v_mov_b32_e32 v4, s20
	v_cndmask_b32_e64 v2, v2, v4, s[6:7]
	v_lshlrev_b64 v[4:5], 9, v[104:105]
	v_lshl_add_u64 v[2:3], v[2:3], 0, v[4:5]
	v_lshlrev_b32_e32 v122, 10, v197
	v_lshl_add_u64 v[2:3], v[2:3], 0, v[108:109]
	v_or_b32_e32 v106, v122, v196
	global_load_dwordx4 v[82:85], v[2:3], off
	v_lshlrev_b32_e32 v2, 4, v106
	v_or_b32_e32 v123, 0x100, v122
	global_load_dwordx4 v[86:89], v2, s[18:19]
	global_load_dwordx4 v[90:93], v2, s[18:19] offset:1024
	global_load_dwordx4 v[94:97], v2, s[18:19] offset:2048
	global_load_dwordx4 v[98:101], v2, s[18:19] offset:3072
	v_or_b32_e32 v2, v123, v196
	v_or_b32_e32 v124, 0x140, v122
	v_lshlrev_b32_e32 v131, 4, v2
	v_or_b32_e32 v2, v124, v196
	v_or_b32_e32 v125, 0x180, v122
	v_lshlrev_b32_e32 v132, 4, v2
	v_or_b32_e32 v2, v125, v196
	v_or_b32_e32 v126, 0x1c0, v122
	v_lshlrev_b32_e32 v133, 4, v2
	v_or_b32_e32 v2, v126, v196
	v_or_b32_e32 v127, 0x200, v122
	v_lshlrev_b32_e32 v134, 4, v2
	v_or_b32_e32 v2, v127, v196
	v_or_b32_e32 v128, 0x240, v122
	v_lshlrev_b32_e32 v135, 4, v2
	v_or_b32_e32 v2, v128, v196
	v_or_b32_e32 v129, 0x280, v122
	v_lshlrev_b32_e32 v137, 4, v2
	v_or_b32_e32 v2, v129, v196
	v_or_b32_e32 v130, 0x2c0, v122
	v_lshlrev_b32_e32 v136, 4, v2
	v_or_b32_e32 v2, v130, v196
	v_or_b32_e32 v192, 0x300, v122
	v_lshlrev_b32_e32 v142, 4, v2
	v_or_b32_e32 v2, v192, v196
	v_or_b32_e32 v202, 0x340, v122
	v_lshlrev_b32_e32 v143, 4, v2
	v_or_b32_e32 v2, v202, v196
	v_or_b32_e32 v203, 0x380, v122
	v_lshlrev_b32_e32 v144, 4, v2
	v_or_b32_e32 v2, v203, v196
	v_or_b32_e32 v204, 0x3c0, v122
	s_movk_i32 s2, 0xc8
	v_bfe_u32 v1, v0, 3, 3
	v_lshlrev_b32_e32 v145, 4, v2
	v_or_b32_e32 v2, v204, v196
	v_mad_i64_i32 v[182:183], s[2:3], v104, s2, 0
	v_lshlrev_b32_e32 v150, 4, v2
	v_lshl_add_u64 v[2:3], v[182:183], 2, s[16:17]
	v_lshlrev_b32_e32 v108, 2, v1
	v_lshlrev_b32_e32 v1, 9, v197
	v_lshl_add_u64 v[16:17], v[2:3], 0, v[108:109]
	v_or_b32_e32 v3, v1, v196
	v_or_b32_e32 v2, 0x100, v1
	v_lshlrev_b32_e32 v3, 4, v3
	global_load_dwordx4 v[110:113], v131, s[18:19]
	global_load_dwordx4 v[114:117], v132, s[18:19]
	global_load_dwordx4 v[118:121], v133, s[18:19]
	global_load_dwordx4 v[138:141], v134, s[18:19]
	global_load_dwordx4 v[146:149], v135, s[18:19]
	global_load_dwordx4 v[152:155], v137, s[18:19]
	global_load_dwordx4 v[156:159], v136, s[18:19]
	global_load_dwordx4 v[160:163], v142, s[18:19]
	global_load_dwordx4 v[164:167], v143, s[18:19]
	global_load_dwordx4 v[168:171], v144, s[18:19]
	global_load_dwordx4 v[172:175], v145, s[18:19]
	global_load_dwordx4 v[176:179], v150, s[18:19]
	global_load_dwordx4 v[186:189], v3, s[4:5]
	global_load_dwordx4 v[206:209], v3, s[4:5] offset:1024
	global_load_dwordx4 v[210:213], v3, s[4:5] offset:2048
	global_load_dwordx4 v[214:217], v3, s[4:5] offset:3072
	v_or_b32_e32 v3, v2, v196
	v_or_b32_e32 v4, 0x140, v1
	v_lshlrev_b32_e32 v3, 4, v3
	v_or_b32_e32 v5, v4, v196
	v_or_b32_e32 v10, 0x180, v1
	v_or_b32_e32 v12, 0x1000, v196
	v_lshlrev_b32_e32 v5, 4, v5
	global_load_dwordx4 v[42:45], v3, s[4:5]
	global_load_dwordx4 v[50:53], v5, s[4:5]
	v_or_b32_e32 v3, v10, v196
	v_or_b32_e32 v11, 0x1c0, v1
	v_or_b32_e32 v1, v1, v12
	v_lshlrev_b32_e32 v3, 4, v3
	v_or_b32_e32 v5, v11, v196
	v_lshlrev_b32_e32 v1, 4, v1
	v_lshlrev_b32_e32 v5, 4, v5
	global_load_dwordx4 v[78:81], v3, s[4:5]
	global_load_dwordx4 v[74:77], v5, s[4:5]
	global_load_dwordx4 v[38:41], v1, s[4:5]
	global_load_dwordx4 v[30:33], v1, s[4:5] offset:1024
	global_load_dwordx4 v[22:25], v1, s[4:5] offset:2048
	global_load_dwordx4 v[26:29], v1, s[4:5] offset:3072
	v_or_b32_e32 v1, v2, v12
	v_or_b32_e32 v2, v4, v12
	v_lshlrev_b32_e32 v1, 4, v1
	v_lshlrev_b32_e32 v6, 4, v2
	global_load_dwordx4 v[2:5], v1, s[4:5]
	s_nop 0
	global_load_dwordx4 v[6:9], v6, s[4:5]
	v_or_b32_e32 v1, v10, v12
	v_or_b32_e32 v10, v11, v12
	v_lshlrev_b32_e32 v1, 4, v1
	v_lshlrev_b32_e32 v10, 4, v10
	global_load_dwordx4 v[18:21], v1, s[4:5]
	s_nop 0
	global_load_dwordx4 v[10:13], v10, s[4:5]
	s_nop 0
	global_load_dword v107, v[16:17], off
	global_load_dwordx4 v[70:73], v[14:15], off sc0 sc1 nt
	global_load_dwordx4 v[66:69], v[14:15], off offset:512 sc0 sc1 nt
	global_load_dwordx4 v[62:65], v[14:15], off offset:1024 sc0 sc1 nt
	global_load_dwordx4 v[58:61], v[14:15], off offset:1536 sc0 sc1 nt
	global_load_dwordx4 v[54:57], v[14:15], off offset:2048 sc0 sc1 nt
	global_load_dwordx4 v[46:49], v[14:15], off offset:2560 sc0 sc1 nt
	global_load_dwordx4 v[34:37], v[14:15], off offset:3072 sc0 sc1 nt
	s_nop 0
	global_load_dwordx4 v[14:17], v[14:15], off offset:3584 sc0 sc1 nt
	v_bfe_u32 v195, v0, 4, 2
	v_and_b32_e32 v1, 15, v0
	s_waitcnt vmcnt(41)
	v_cvt_pk_f16_f32 v85, v84, v85
	v_cvt_pk_f16_f32 v84, v82, v83
	v_lshlrev_b32_e32 v82, 3, v196
	s_movk_i32 s2, 0x410
	v_mad_u32_u24 v185, v197, s2, v82
	v_and_b32_e32 v82, 7, v0
	v_and_b32_e32 v194, 48, v0
	v_mad_u32_u24 v105, v82, s2, v194
	ds_write_b64 v185, v[84:85]
	s_waitcnt lgkmcnt(0)
	s_barrier
	ds_read_b128 v[82:85], v105
	ds_read_b128 v[198:201], v105 offset:64
	s_waitcnt vmcnt(40) lgkmcnt(1)
	v_mfma_f32_16x16x32_f16 v[86:89], v[82:85], v[86:89], 0
	s_movk_i32 s2, 0x840
	s_waitcnt vmcnt(32)
	v_mfma_f32_16x16x32_f16 v[82:85], v[82:85], v[146:149], 0
	s_waitcnt lgkmcnt(0)
	v_mfma_f32_16x16x32_f16 v[86:89], v[198:201], v[90:93], v[86:89]
	ds_read_b128 v[90:93], v105 offset:128
	ds_read_b128 v[146:149], v105 offset:192
	s_waitcnt vmcnt(31)
	v_mfma_f32_16x16x32_f16 v[82:85], v[198:201], v[152:155], v[82:85]
	v_lshlrev_b32_e32 v200, 7, v197
	v_lshl_or_b32 v109, v1, 2, v200
	v_add_u32_e32 v109, 0x4100, v109
	s_waitcnt lgkmcnt(1)
	v_mfma_f32_16x16x32_f16 v[86:89], v[90:93], v[94:97], v[86:89]
	ds_read_b128 v[94:97], v105 offset:320
	v_lshl_add_u32 v109, v195, 13, v109
	s_waitcnt vmcnt(30)
	v_mfma_f32_16x16x32_f16 v[82:85], v[90:93], v[156:159], v[82:85]
	ds_read_b128 v[90:93], v105 offset:256
	s_waitcnt lgkmcnt(2)
	v_mfma_f32_16x16x32_f16 v[86:89], v[146:149], v[98:101], v[86:89]
	ds_read_b128 v[98:101], v105 offset:384
	s_waitcnt vmcnt(29)
	v_mfma_f32_16x16x32_f16 v[82:85], v[146:149], v[160:163], v[82:85]
	s_waitcnt lgkmcnt(1)
	v_mfma_f32_16x16x32_f16 v[86:89], v[90:93], v[110:113], v[86:89]
	ds_read_b128 v[110:113], v105 offset:448
	v_and_b32_e32 v105, 0x1c0, v0
	v_mfma_f32_16x16x32_f16 v[86:89], v[94:97], v[114:117], v[86:89]
	s_waitcnt vmcnt(28)
	v_mfma_f32_16x16x32_f16 v[82:85], v[90:93], v[164:167], v[82:85]
	v_mad_u32_u24 v90, v195, s2, v105
	v_lshl_or_b32 v105, v1, 1, v90
	s_movk_i32 s2, 0x210
	s_waitcnt lgkmcnt(1)
	v_mfma_f32_16x16x32_f16 v[86:89], v[98:101], v[118:121], v[86:89]
	s_waitcnt vmcnt(27)
	v_mfma_f32_16x16x32_f16 v[82:85], v[94:97], v[168:171], v[82:85]
	s_waitcnt lgkmcnt(0)
	v_mfma_f32_16x16x32_f16 v[86:89], v[110:113], v[138:141], v[86:89]
	s_waitcnt vmcnt(26)
	v_mfma_f32_16x16x32_f16 v[82:85], v[98:101], v[172:175], v[82:85]
	s_waitcnt vmcnt(25)
	v_mfma_f32_16x16x32_f16 v[82:85], v[110:113], v[176:179], v[82:85]
	s_nop 3
	v_cvt_f16_f32_e32 v86, v86
	ds_write_b16 v105, v86 offset:58624
	v_cvt_f16_f32_e32 v86, v87
	s_nop 0
	v_cvt_f16_f32_e32 v82, v82
	v_cvt_f16_f32_e32 v87, v88
	v_cvt_f16_f32_e32 v83, v83
	v_cvt_f16_f32_e32 v88, v89
	v_cvt_f16_f32_e32 v84, v84
	v_cvt_f16_f32_e32 v85, v85
	ds_write_b16 v105, v86 offset:59152
	ds_write_b16 v105, v87 offset:59680
	ds_write_b16 v105, v88 offset:60208
	ds_write_b16 v105, v82 offset:58656
	ds_write_b16 v105, v83 offset:59184
	ds_write_b16 v105, v84 offset:59712
	ds_write_b16 v105, v85 offset:60240
	v_mov_b32_e32 v82, 0xe500
	v_mad_u32_u24 v82, v1, s2, v82
	v_add_u32_e32 v198, v82, v194
	s_waitcnt lgkmcnt(0)
	s_barrier
	ds_read_b128 v[82:85], v198
	ds_read_b128 v[86:89], v198 offset:64
	s_waitcnt vmcnt(24) lgkmcnt(1)
	v_mfma_f32_16x16x32_f16 v[94:97], v[82:85], v[186:189], 0
	ds_read_b128 v[90:93], v198 offset:128
	s_waitcnt vmcnt(23) lgkmcnt(1)
	v_mfma_f32_16x16x32_f16 v[98:101], v[86:89], v[206:209], v[94:97]
	s_nop 4
	ds_read_b128 v[94:97], v198 offset:192
	s_waitcnt vmcnt(22) lgkmcnt(1)
	v_mfma_f32_16x16x32_f16 v[98:101], v[90:93], v[210:213], v[98:101]
	s_waitcnt vmcnt(21) lgkmcnt(0)
	v_mfma_f32_16x16x32_f16 v[98:101], v[94:97], v[214:217], v[98:101]
	s_and_saveexec_b64 s[2:3], s[6:7]
	s_cbranch_execz .LBB1_2
	s_nop 5
	v_mul_f32_e32 v98, 0x3e0293ee, v98
	v_mul_f32_e32 v99, 0x3e0293ee, v99
	ds_write2st64_b32 v109, v98, v99 offset1:8
	v_mul_f32_e32 v98, 0x3e0293ee, v100
	v_mul_f32_e32 v99, 0x3e0293ee, v101
	ds_write2st64_b32 v109, v98, v99 offset0:16 offset1:24

.LBB1_9:
	v_add_co_u32_e64 v2, s[0:1], s35, v112
	s_waitcnt vmcnt(6) lgkmcnt(0)
	v_mul_f32_e32 v4, v10, v66
	v_addc_co_u32_e64 v3, s[0:1], -1, v113, s[0:1]
	global_load_dwordx4 v[102:105], v[2:3], off offset:-3584 sc0 sc1 nt
	global_load_dwordx4 v[98:101], v[2:3], off offset:-3072 sc0 sc1 nt
	global_load_dwordx4 v[94:97], v[2:3], off offset:-2560 sc0 sc1 nt
	global_load_dwordx4 v[90:93], v[2:3], off offset:-2048 sc0 sc1 nt
	global_load_dwordx4 v[86:89], v[2:3], off offset:-1536 sc0 sc1 nt
	global_load_dwordx4 v[82:85], v[2:3], off offset:-1024 sc0 sc1 nt
	global_load_dwordx4 v[78:81], v[2:3], off offset:-512 sc0 sc1 nt
	global_load_dwordx4 v[74:77], v[112:113], off offset:-4096 sc0 sc1 nt
	global_load_dword v121, v[110:111], off
	v_mul_f32_e32 v2, v10, v70
	s_waitcnt vmcnt(14)
	v_mul_f32_e32 v18, v10, v62
	s_waitcnt vmcnt(13)
	v_mul_f32_e32 v20, v10, v58
	s_waitcnt vmcnt(12)
	v_mul_f32_e32 v22, v10, v54
	s_waitcnt vmcnt(11)
	v_mul_f32_e32 v24, v10, v46
	s_waitcnt vmcnt(10)
	v_mul_f32_e32 v26, v10, v34
	s_waitcnt vmcnt(9)
	v_mul_f32_e32 v28, v10, v14
	v_fmac_f32_e32 v2, v71, v11
	v_mul_f32_e32 v3, v6, v70
	v_fmac_f32_e32 v4, v67, v11
	v_mul_f32_e32 v5, v6, v66
	v_fmac_f32_e32 v18, v63, v11
	v_mul_f32_e32 v19, v6, v62
	v_fmac_f32_e32 v20, v59, v11
	v_mul_f32_e32 v21, v6, v58
	v_fmac_f32_e32 v22, v55, v11
	v_mul_f32_e32 v23, v6, v54
	v_fmac_f32_e32 v24, v47, v11
	v_mul_f32_e32 v25, v6, v46
	v_fmac_f32_e32 v26, v35, v11
	v_mul_f32_e32 v27, v6, v34
	v_fmac_f32_e32 v28, v15, v11
	v_mul_f32_e32 v29, v6, v14
	v_fmac_f32_e32 v2, v72, v12
	v_fmac_f32_e32 v3, v71, v7
	v_fmac_f32_e32 v4, v68, v12
	v_fmac_f32_e32 v5, v67, v7
	v_fmac_f32_e32 v18, v64, v12
	v_fmac_f32_e32 v19, v63, v7
	v_fmac_f32_e32 v20, v60, v12
	v_fmac_f32_e32 v21, v59, v7
	v_fmac_f32_e32 v22, v56, v12
	v_fmac_f32_e32 v23, v55, v7
	v_fmac_f32_e32 v24, v48, v12
	v_fmac_f32_e32 v25, v47, v7
	v_fmac_f32_e32 v26, v36, v12
	v_fmac_f32_e32 v27, v35, v7
	v_fmac_f32_e32 v28, v16, v12
	v_fmac_f32_e32 v29, v15, v7
	v_fmac_f32_e32 v2, v73, v13
	v_fmac_f32_e32 v3, v72, v8
	v_fmac_f32_e32 v4, v69, v13
	v_fmac_f32_e32 v5, v68, v8
	v_fmac_f32_e32 v18, v65, v13
	v_fmac_f32_e32 v19, v64, v8
	v_fmac_f32_e32 v20, v61, v13
	v_fmac_f32_e32 v21, v60, v8
	v_fmac_f32_e32 v22, v57, v13
	v_fmac_f32_e32 v23, v56, v8
	v_fmac_f32_e32 v24, v49, v13
	v_fmac_f32_e32 v25, v48, v8
	v_fmac_f32_e32 v26, v37, v13
	v_fmac_f32_e32 v27, v36, v8
	v_fmac_f32_e32 v28, v17, v13
	v_fmac_f32_e32 v29, v16, v8
	v_fmac_f32_e32 v3, v73, v9
	v_fmac_f32_e32 v5, v69, v9
	v_fmac_f32_e32 v19, v65, v9
	v_fmac_f32_e32 v21, v61, v9
	v_fmac_f32_e32 v23, v57, v9
	v_fmac_f32_e32 v25, v49, v9
	v_fmac_f32_e32 v27, v37, v9
	v_fmac_f32_e32 v29, v17, v9
	v_permlane32_swap_b32_e32 v2, v22
	v_permlane32_swap_b32_e32 v4, v24
	v_permlane32_swap_b32_e32 v18, v26
	v_permlane32_swap_b32_e32 v20, v28
	v_add_f32_e32 v2, v2, v22
	v_permlane32_swap_b32_e32 v3, v23
	v_add_f32_e32 v4, v4, v24
	v_permlane32_swap_b32_e32 v5, v25
	v_add_f32_e32 v18, v18, v26
	v_permlane32_swap_b32_e32 v19, v27
	v_add_f32_e32 v20, v20, v28
	v_permlane32_swap_b32_e32 v21, v29
	v_add_f32_e32 v3, v3, v23
	v_add_f32_e32 v5, v5, v25
	v_add_f32_e32 v19, v19, v27
	v_add_f32_e32 v21, v21, v29
	v_permlane16_swap_b32_e32 v2, v18
	v_permlane16_swap_b32_e32 v4, v20
	v_add_f32_e32 v2, v2, v18
	v_permlane16_swap_b32_e32 v3, v19
	v_add_f32_e32 v4, v4, v20
	v_permlane16_swap_b32_e32 v5, v21
	v_add_f32_e32 v3, v3, v19
	v_add_f32_e32 v5, v5, v21
	v_add_f32_dpp v2, v2, v2 row_ror:8 row_mask:0xf bank_mask:0xf bound_ctrl:1
	v_add_f32_dpp v4, v4, v4 row_ror:8 row_mask:0xf bank_mask:0xf bound_ctrl:1
	v_cndmask_b32_e64 v2, v4, v2, s[4:5]
	v_add_f32_dpp v3, v3, v3 row_ror:8 row_mask:0xf bank_mask:0xf bound_ctrl:1
	v_add_f32_dpp v4, v5, v5 row_ror:8 row_mask:0xf bank_mask:0xf bound_ctrl:1
	v_cndmask_b32_e64 v3, v4, v3, s[4:5]
	v_add_f32_dpp v2, v2, v2 row_half_mirror row_mask:0xf bank_mask:0xf bound_ctrl:1
	v_cmp_eq_u32_e64 s[0:1], 0, v107
	v_add_f32_dpp v3, v3, v3 row_half_mirror row_mask:0xf bank_mask:0xf bound_ctrl:1
	v_cndmask_b32_e64 v2, v3, v2, s[2:3]
	s_nop 1
	v_add_f32_dpp v2, v2, v2 quad_perm:[2,3,0,1] row_mask:0xf bank_mask:0xf bound_ctrl:1
	s_nop 1
	v_add_f32_dpp v2, v2, v2 quad_perm:[1,0,3,2] row_mask:0xf bank_mask:0xf bound_ctrl:1
	v_cndmask_b32_e64 v2, v119, v2, s[0:1]
	s_and_saveexec_b64 s[0:1], vcc
	ds_write_b32 v118, v2
	s_or_b64 exec, exec, s[0:1]
	v_mov_b32_dpp v3, v2 row_ror:8 row_mask:0xf bank_mask:0xf bound_ctrl:1
	v_max_f32_e32 v3, v3, v3
	v_max_f32_e32 v4, v2, v2
	v_max_f32_e32 v3, v4, v3
	v_mov_b32_e32 v4, v3
	s_nop 1
	v_permlane16_swap_b32_e32 v3, v4
	v_max_f32_e32 v4, v4, v4
	v_max_f32_e32 v3, v3, v3
	v_max_f32_e32 v3, v3, v4
	v_mov_b32_e32 v4, v3
	s_nop 1
	v_permlane32_swap_b32_e32 v3, v4
	v_max3_f32 v139, v120, v3, v4
	v_sub_f32_e32 v3, v120, v139
	v_sub_f32_e32 v2, v2, v139
	v_exp_f32_e32 v120, v3
	v_exp_f32_e32 v138, v2
	global_load_dwordx4 v[50:53], v[112:113], off offset:-3584 sc0 sc1 nt
	global_load_dwordx4 v[42:45], v[112:113], off offset:-3072 sc0 sc1 nt
	global_load_dwordx4 v[38:41], v[112:113], off offset:-2560 sc0 sc1 nt
	global_load_dwordx4 v[30:33], v[112:113], off offset:-2048 sc0 sc1 nt
	global_load_dwordx4 v[26:29], v[112:113], off offset:-1536 sc0 sc1 nt
	global_load_dwordx4 v[22:25], v[112:113], off offset:-1024 sc0 sc1 nt
	global_load_dwordx4 v[18:21], v[112:113], off offset:-512 sc0 sc1 nt
	global_load_dwordx4 v[2:5], v[112:113], off sc0 sc1 nt
	global_load_dword v107, v[110:111], off offset:32
	s_waitcnt vmcnt(17)
	v_mul_f32_e32 v140, v10, v102
	s_waitcnt vmcnt(16)
	v_mul_f32_e32 v146, v10, v98
	s_waitcnt vmcnt(15)
	v_mul_f32_e32 v148, v10, v94
	s_waitcnt vmcnt(14)
	v_mul_f32_e32 v151, v10, v90
	s_waitcnt vmcnt(13)
	v_mul_f32_e32 v153, v10, v86
	s_waitcnt vmcnt(12)
	v_mul_f32_e32 v155, v10, v82
	s_waitcnt vmcnt(11)
	v_mul_f32_e32 v157, v10, v78
	s_waitcnt vmcnt(10)
	v_mul_f32_e32 v159, v10, v74
	v_fmac_f32_e32 v140, v103, v11
	v_mul_f32_e32 v141, v6, v102
	v_fmac_f32_e32 v146, v99, v11
	v_mul_f32_e32 v147, v6, v98
	v_fmac_f32_e32 v148, v95, v11
	v_mul_f32_e32 v149, v6, v94
	v_fmac_f32_e32 v151, v91, v11
	v_mul_f32_e32 v152, v6, v90
	v_fmac_f32_e32 v153, v87, v11
	v_mul_f32_e32 v154, v6, v86
	v_fmac_f32_e32 v155, v83, v11
	v_mul_f32_e32 v156, v6, v82
	v_fmac_f32_e32 v157, v79, v11
	v_mul_f32_e32 v158, v6, v78
	v_fmac_f32_e32 v159, v75, v11
	v_mul_f32_e32 v160, v6, v74
	v_fmac_f32_e32 v140, v104, v12
	v_fmac_f32_e32 v141, v103, v7
	v_fmac_f32_e32 v146, v100, v12
	v_fmac_f32_e32 v147, v99, v7
	v_fmac_f32_e32 v148, v96, v12
	v_fmac_f32_e32 v149, v95, v7
	v_fmac_f32_e32 v151, v92, v12
	v_fmac_f32_e32 v152, v91, v7
	v_fmac_f32_e32 v153, v88, v12
	v_fmac_f32_e32 v154, v87, v7
	v_fmac_f32_e32 v155, v84, v12
	v_fmac_f32_e32 v156, v83, v7
	v_fmac_f32_e32 v157, v80, v12
	v_fmac_f32_e32 v158, v79, v7
	v_fmac_f32_e32 v159, v76, v12
	v_fmac_f32_e32 v160, v75, v7
	v_fmac_f32_e32 v140, v105, v13
	v_fmac_f32_e32 v141, v104, v8
	v_fmac_f32_e32 v146, v101, v13
	v_fmac_f32_e32 v147, v100, v8
	v_fmac_f32_e32 v148, v97, v13
	v_fmac_f32_e32 v149, v96, v8
	v_fmac_f32_e32 v151, v93, v13
	v_fmac_f32_e32 v152, v92, v8
	v_fmac_f32_e32 v153, v89, v13
	v_fmac_f32_e32 v154, v88, v8
	v_fmac_f32_e32 v155, v85, v13
	v_fmac_f32_e32 v156, v84, v8
	v_fmac_f32_e32 v157, v81, v13
	v_fmac_f32_e32 v158, v80, v8
	v_fmac_f32_e32 v159, v77, v13
	v_fmac_f32_e32 v160, v76, v8
	v_fmac_f32_e32 v141, v105, v9
	v_fmac_f32_e32 v147, v101, v9
	v_fmac_f32_e32 v149, v97, v9
	v_fmac_f32_e32 v152, v93, v9
	v_fmac_f32_e32 v154, v89, v9
	v_fmac_f32_e32 v156, v85, v9
	v_fmac_f32_e32 v158, v81, v9
	v_fmac_f32_e32 v160, v77, v9
	v_permlane32_swap_b32_e32 v140, v153
	v_permlane32_swap_b32_e32 v146, v155
	v_permlane32_swap_b32_e32 v148, v157
	v_permlane32_swap_b32_e32 v151, v159
	v_add_f32_e32 v140, v140, v153
	v_permlane32_swap_b32_e32 v141, v154
	v_add_f32_e32 v146, v146, v155
	v_permlane32_swap_b32_e32 v147, v156
	v_add_f32_e32 v148, v148, v157
	v_permlane32_swap_b32_e32 v149, v158
	v_add_f32_e32 v151, v151, v159
	v_permlane32_swap_b32_e32 v152, v160
	v_add_f32_e32 v141, v141, v154
	v_add_f32_e32 v147, v147, v156
	v_add_f32_e32 v149, v149, v158
	v_add_f32_e32 v152, v152, v160
	v_permlane16_swap_b32_e32 v140, v148
	v_permlane16_swap_b32_e32 v146, v151
	v_add_f32_e32 v140, v140, v148
	v_permlane16_swap_b32_e32 v141, v149
	v_add_f32_e32 v146, v146, v151
	v_permlane16_swap_b32_e32 v147, v152
	v_add_f32_e32 v141, v141, v149
	v_add_f32_e32 v147, v147, v152
	v_add_f32_dpp v140, v140, v140 row_ror:8 row_mask:0xf bank_mask:0xf bound_ctrl:1
	v_add_f32_dpp v146, v146, v146 row_ror:8 row_mask:0xf bank_mask:0xf bound_ctrl:1
	v_cndmask_b32_e64 v140, v146, v140, s[4:5]
	v_add_f32_dpp v141, v141, v141 row_ror:8 row_mask:0xf bank_mask:0xf bound_ctrl:1
	v_add_f32_dpp v146, v147, v147 row_ror:8 row_mask:0xf bank_mask:0xf bound_ctrl:1
	v_cndmask_b32_e64 v141, v146, v141, s[4:5]
	v_add_f32_dpp v140, v140, v140 row_half_mirror row_mask:0xf bank_mask:0xf bound_ctrl:1
	s_waitcnt vmcnt(9)
	v_cmp_eq_u32_e64 s[0:1], 0, v121
	v_add_f32_dpp v141, v141, v141 row_half_mirror row_mask:0xf bank_mask:0xf bound_ctrl:1
	v_cndmask_b32_e64 v140, v141, v140, s[2:3]
	v_readlane_b32 s66, v120, 0
	v_readlane_b32 s64, v120, 4
	v_add_f32_dpp v140, v140, v140 quad_perm:[2,3,0,1] row_mask:0xf bank_mask:0xf bound_ctrl:1
	v_readlane_b32 s62, v138, 0
	v_readlane_b32 s60, v138, 4
	v_add_f32_dpp v140, v140, v140 quad_perm:[1,0,3,2] row_mask:0xf bank_mask:0xf bound_ctrl:1
	v_readlane_b32 s58, v138, 8
	v_readlane_b32 s56, v138, 12
	v_readlane_b32 s54, v138, 16
	v_readlane_b32 s52, v138, 20
	v_readlane_b32 s50, v138, 24
	v_readlane_b32 s48, v138, 28
	v_readlane_b32 s46, v138, 32
	v_readlane_b32 s44, v138, 36
	v_readlane_b32 s42, v138, 40
	v_readlane_b32 s40, v138, 44
	v_readlane_b32 s38, v138, 48
	v_readlane_b32 s36, v138, 52
	v_readlane_b32 s34, v138, 56
	v_readlane_b32 s30, v138, 60
	v_cndmask_b32_e64 v121, v119, v140, s[0:1]
	s_and_saveexec_b64 s[0:1], vcc
	ds_write_b32 v118, v121 offset:32
	s_or_b64 exec, exec, s[0:1]
	v_cmp_neq_f32_e64 s[0:1], s66, 1.0
	v_cmp_neq_f32_e64 s[68:69], s64, 1.0
	v_pk_mul_f32 v[140:141], v[114:115], s[66:67] op_sel_hi:[1,0]
	v_pk_mul_f32 v[146:147], v[116:117], s[66:67] op_sel_hi:[1,0]
	v_pk_mul_f32 v[148:149], v[188:189], s[64:65] op_sel_hi:[1,0]
	s_or_b64 s[0:1], s[0:1], s[68:69]
	v_pk_mul_f32 v[152:153], v[190:191], s[64:65] op_sel_hi:[1,0]
	v_cndmask_b32_e64 v117, v117, v147, s[0:1]
	v_cndmask_b32_e64 v116, v116, v146, s[0:1]
	v_cndmask_b32_e64 v115, v115, v141, s[0:1]
	v_cndmask_b32_e64 v114, v114, v140, s[0:1]
	v_cndmask_b32_e64 v147, v189, v149, s[0:1]
	v_cndmask_b32_e64 v146, v188, v148, s[0:1]
	v_cndmask_b32_e64 v141, v191, v153, s[0:1]
	v_cndmask_b32_e64 v140, v190, v152, s[0:1]
	v_pk_fma_f32 v[114:115], v[72:73], s[62:63], v[114:115] op_sel_hi:[1,0,1]
	v_pk_fma_f32 v[72:73], v[72:73], s[60:61], v[146:147] op_sel_hi:[1,0,1]
	v_pk_fma_f32 v[116:117], v[70:71], s[62:63], v[116:117] op_sel_hi:[1,0,1]
	v_pk_fma_f32 v[70:71], v[70:71], s[60:61], v[140:141] op_sel_hi:[1,0,1]
	v_pk_fma_f32 v[114:115], v[68:69], s[58:59], v[114:115] op_sel_hi:[1,0,1]
	v_pk_fma_f32 v[68:69], v[68:69], s[56:57], v[72:73] op_sel_hi:[1,0,1]
	v_pk_fma_f32 v[116:117], v[66:67], s[58:59], v[116:117] op_sel_hi:[1,0,1]
	v_pk_fma_f32 v[66:67], v[66:67], s[56:57], v[70:71] op_sel_hi:[1,0,1]
	v_pk_fma_f32 v[70:71], v[64:65], s[54:55], v[114:115] op_sel_hi:[1,0,1]
	v_pk_fma_f32 v[64:65], v[64:65], s[52:53], v[68:69] op_sel_hi:[1,0,1]
	v_pk_fma_f32 v[72:73], v[62:63], s[54:55], v[116:117] op_sel_hi:[1,0,1]
	v_pk_fma_f32 v[62:63], v[62:63], s[52:53], v[66:67] op_sel_hi:[1,0,1]
	v_pk_fma_f32 v[68:69], v[60:61], s[50:51], v[70:71] op_sel_hi:[1,0,1]
	v_pk_fma_f32 v[60:61], v[60:61], s[48:49], v[64:65] op_sel_hi:[1,0,1]
	v_pk_fma_f32 v[66:67], v[58:59], s[50:51], v[72:73] op_sel_hi:[1,0,1]
	v_pk_fma_f32 v[58:59], v[58:59], s[48:49], v[62:63] op_sel_hi:[1,0,1]
	v_pk_fma_f32 v[62:63], v[56:57], s[46:47], v[68:69] op_sel_hi:[1,0,1]
	v_pk_fma_f32 v[56:57], v[56:57], s[44:45], v[60:61] op_sel_hi:[1,0,1]
	v_pk_fma_f32 v[64:65], v[54:55], s[46:47], v[66:67] op_sel_hi:[1,0,1]
	v_pk_fma_f32 v[54:55], v[54:55], s[44:45], v[58:59] op_sel_hi:[1,0,1]
	v_pk_fma_f32 v[60:61], v[48:49], s[42:43], v[62:63] op_sel_hi:[1,0,1]
	v_pk_fma_f32 v[48:49], v[48:49], s[40:41], v[56:57] op_sel_hi:[1,0,1]
	v_pk_fma_f32 v[58:59], v[46:47], s[42:43], v[64:65] op_sel_hi:[1,0,1]
	v_pk_fma_f32 v[46:47], v[46:47], s[40:41], v[54:55] op_sel_hi:[1,0,1]
	v_pk_fma_f32 v[54:55], v[36:37], s[38:39], v[60:61] op_sel_hi:[1,0,1]
	v_pk_fma_f32 v[36:37], v[36:37], s[36:37], v[48:49] op_sel_hi:[1,0,1]
	v_mov_b32_dpp v48, v121 row_ror:8 row_mask:0xf bank_mask:0xf bound_ctrl:1
	v_max_f32_e32 v48, v48, v48
	v_max_f32_e32 v49, v121, v121
	v_max_f32_e32 v48, v49, v48
	v_mov_b32_e32 v49, v48
	s_nop 1
	v_permlane16_swap_b32_e32 v48, v49
	v_max_f32_e32 v49, v49, v49
	v_max_f32_e32 v48, v48, v48
	v_max_f32_e32 v48, v48, v49
	v_mov_b32_e32 v49, v48
	s_nop 1
	v_permlane32_swap_b32_e32 v48, v49
	v_fmac_f32_e32 v138, v187, v120
	v_max3_f32 v120, v139, v48, v49
	v_pk_fma_f32 v[56:57], v[34:35], s[38:39], v[58:59] op_sel_hi:[1,0,1]
	v_sub_f32_e32 v48, v139, v120
	v_pk_fma_f32 v[34:35], v[34:35], s[36:37], v[46:47] op_sel_hi:[1,0,1]
	v_pk_fma_f32 v[46:47], v[14:15], s[34:35], v[56:57] op_sel_hi:[1,0,1]
	v_exp_f32_e32 v56, v48
	v_sub_f32_e32 v48, v121, v120
	v_exp_f32_e32 v58, v48
	v_pk_fma_f32 v[48:49], v[16:17], s[34:35], v[54:55] op_sel_hi:[1,0,1]
	v_pk_fma_f32 v[14:15], v[14:15], s[30:31], v[34:35] op_sel_hi:[1,0,1]
	v_pk_fma_f32 v[16:17], v[16:17], s[30:31], v[36:37] op_sel_hi:[1,0,1]
	v_readlane_b32 s0, v56, 0
	v_readlane_b32 s30, v56, 4
	v_fma_f32 v187, v138, v56, v58
	v_cmp_neq_f32_e64 s[36:37], s0, 1.0
	v_cmp_neq_f32_e64 s[38:39], s30, 1.0
	v_pk_mul_f32 v[34:35], v[46:47], s[0:1] op_sel_hi:[1,0]
	v_pk_mul_f32 v[36:37], v[48:49], s[0:1] op_sel_hi:[1,0]
	v_pk_mul_f32 v[54:55], v[14:15], s[30:31] op_sel_hi:[1,0]
	v_pk_mul_f32 v[56:57], v[16:17], s[30:31] op_sel_hi:[1,0]
	s_or_b64 s[0:1], s[36:37], s[38:39]
	v_cndmask_b32_e64 v37, v49, v37, s[0:1]
	v_cndmask_b32_e64 v36, v48, v36, s[0:1]
	v_cndmask_b32_e64 v35, v47, v35, s[0:1]
	v_cndmask_b32_e64 v34, v46, v34, s[0:1]
	v_cndmask_b32_e64 v17, v17, v57, s[0:1]
	v_cndmask_b32_e64 v16, v16, v56, s[0:1]
	v_cndmask_b32_e64 v15, v15, v55, s[0:1]
	v_cndmask_b32_e64 v14, v14, v54, s[0:1]
	v_readlane_b32 s0, v58, 0
	v_readlane_b32 s30, v58, 4
	s_add_i32 s33, s33, 2
	v_pk_fma_f32 v[34:35], v[102:103], s[0:1], v[34:35] op_sel_hi:[1,0,1]
	v_pk_fma_f32 v[36:37], v[104:105], s[0:1], v[36:37] op_sel_hi:[1,0,1]
	v_pk_fma_f32 v[14:15], v[102:103], s[30:31], v[14:15] op_sel_hi:[1,0,1]
	v_pk_fma_f32 v[16:17], v[104:105], s[30:31], v[16:17] op_sel_hi:[1,0,1]
	v_readlane_b32 s0, v58, 8
	v_readlane_b32 s30, v58, 12
	v_lshl_add_u64 v[110:111], v[110:111], 0, 64
	v_pk_fma_f32 v[36:37], v[100:101], s[0:1], v[36:37] op_sel_hi:[1,0,1]
	v_pk_fma_f32 v[34:35], v[98:99], s[0:1], v[34:35] op_sel_hi:[1,0,1]
	v_pk_fma_f32 v[16:17], v[100:101], s[30:31], v[16:17] op_sel_hi:[1,0,1]
	v_pk_fma_f32 v[14:15], v[98:99], s[30:31], v[14:15] op_sel_hi:[1,0,1]
	v_readlane_b32 s0, v58, 16
	v_readlane_b32 s30, v58, 20
	v_add_u32_e32 v118, 64, v118
	v_pk_fma_f32 v[34:35], v[94:95], s[0:1], v[34:35] op_sel_hi:[1,0,1]
	v_pk_fma_f32 v[36:37], v[96:97], s[0:1], v[36:37] op_sel_hi:[1,0,1]
	v_pk_fma_f32 v[14:15], v[94:95], s[30:31], v[14:15] op_sel_hi:[1,0,1]
	v_pk_fma_f32 v[16:17], v[96:97], s[30:31], v[16:17] op_sel_hi:[1,0,1]
	v_readlane_b32 s0, v58, 24
	v_readlane_b32 s30, v58, 28
	s_cmp_gt_u32 s33, 21
	v_pk_fma_f32 v[36:37], v[92:93], s[0:1], v[36:37] op_sel_hi:[1,0,1]
	v_pk_fma_f32 v[34:35], v[90:91], s[0:1], v[34:35] op_sel_hi:[1,0,1]
	v_pk_fma_f32 v[16:17], v[92:93], s[30:31], v[16:17] op_sel_hi:[1,0,1]
	v_pk_fma_f32 v[14:15], v[90:91], s[30:31], v[14:15] op_sel_hi:[1,0,1]
	v_readlane_b32 s0, v58, 32
	v_readlane_b32 s30, v58, 36
	v_lshl_add_u64 v[112:113], v[112:113], 0, s[16:17]
	v_pk_fma_f32 v[34:35], v[86:87], s[0:1], v[34:35] op_sel_hi:[1,0,1]
	v_pk_fma_f32 v[36:37], v[88:89], s[0:1], v[36:37] op_sel_hi:[1,0,1]
	v_pk_fma_f32 v[14:15], v[86:87], s[30:31], v[14:15] op_sel_hi:[1,0,1]
	v_pk_fma_f32 v[16:17], v[88:89], s[30:31], v[16:17] op_sel_hi:[1,0,1]
	v_readlane_b32 s0, v58, 40
	v_readlane_b32 s30, v58, 44
	s_nop 0
	v_pk_fma_f32 v[36:37], v[84:85], s[0:1], v[36:37] op_sel_hi:[1,0,1]
	v_pk_fma_f32 v[34:35], v[82:83], s[0:1], v[34:35] op_sel_hi:[1,0,1]
	v_pk_fma_f32 v[16:17], v[84:85], s[30:31], v[16:17] op_sel_hi:[1,0,1]
	v_pk_fma_f32 v[14:15], v[82:83], s[30:31], v[14:15] op_sel_hi:[1,0,1]
	v_readlane_b32 s0, v58, 48
	v_readlane_b32 s30, v58, 52
	s_nop 0
	v_pk_fma_f32 v[34:35], v[78:79], s[0:1], v[34:35] op_sel_hi:[1,0,1]
	v_pk_fma_f32 v[36:37], v[80:81], s[0:1], v[36:37] op_sel_hi:[1,0,1]
	v_pk_fma_f32 v[14:15], v[78:79], s[30:31], v[14:15] op_sel_hi:[1,0,1]
	v_pk_fma_f32 v[16:17], v[80:81], s[30:31], v[16:17] op_sel_hi:[1,0,1]
	v_readlane_b32 s0, v58, 56
	v_readlane_b32 s30, v58, 60
	s_nop 0
	v_pk_fma_f32 v[114:115], v[76:77], s[0:1], v[36:37] op_sel_hi:[1,0,1]
	v_pk_fma_f32 v[116:117], v[74:75], s[0:1], v[34:35] op_sel_hi:[1,0,1]
	v_pk_fma_f32 v[188:189], v[76:77], s[30:31], v[16:17] op_sel_hi:[1,0,1]
	v_pk_fma_f32 v[190:191], v[74:75], s[30:31], v[14:15] op_sel_hi:[1,0,1]
	s_cbranch_scc1 .LBB1_15
	s_waitcnt vmcnt(8)
	v_mov_b64_e32 v[72:73], v[52:53]
	s_waitcnt vmcnt(7)
	v_mov_b64_e32 v[68:69], v[44:45]
	s_waitcnt vmcnt(6)
	v_mov_b64_e32 v[64:65], v[40:41]
	s_waitcnt vmcnt(5)
	v_mov_b64_e32 v[60:61], v[32:33]
	s_waitcnt vmcnt(4)
	v_mov_b64_e32 v[56:57], v[28:29]
	s_waitcnt vmcnt(3)
	v_mov_b64_e32 v[48:49], v[24:25]
	s_waitcnt vmcnt(2)
	v_mov_b64_e32 v[36:37], v[20:21]
	s_waitcnt vmcnt(1)
	v_mov_b64_e32 v[16:17], v[4:5]
	v_mov_b64_e32 v[70:71], v[50:51]
	v_mov_b64_e32 v[66:67], v[42:43]
	v_mov_b64_e32 v[62:63], v[38:39]
	v_mov_b64_e32 v[58:59], v[30:31]
	v_mov_b64_e32 v[54:55], v[26:27]
	v_mov_b64_e32 v[46:47], v[22:23]
	v_mov_b64_e32 v[34:35], v[18:19]
	v_mov_b64_e32 v[14:15], v[2:3]
	s_branch .LBB1_9
